# speedup vs baseline: 1.0025x; 1.0025x over previous
.LBB3_2:
	s_or_b64 exec, exec, s[2:3]
	s_load_dwordx2 s[20:21], s[0:1], 0x58
	s_load_dwordx2 s[24:25], s[0:1], 0x28
	s_load_dwordx2 s[22:23], s[0:1], 0x40
	v_lshlrev_b32_e32 v49, 3, v44
	v_lshlrev_b32_e32 v86, 5, v44
	s_waitcnt lgkmcnt(0)
	global_load_dwordx4 v[78:81], v86, s[24:25]
	global_load_dwordx4 v[82:85], v86, s[24:25] offset:16
	v_and_b32_e32 v43, 63, v0
	v_lshlrev_b32_e32 v47, 4, v44
	v_and_b32_e32 v45, 48, v0
	v_cmp_gt_i32_e32 vcc, v48, v51
	v_mov_b32_e32 v32, 0
	v_mov_b32_e32 v35, 0
	v_mov_b32_e32 v34, 0
	v_mov_b32_e32 v37, 0
	v_mov_b32_e32 v36, 0
	v_mov_b32_e32 v39, 0
	v_mov_b32_e32 v38, 0
	v_mov_b32_e32 v64, 0
	s_and_saveexec_b64 s[28:29], vcc
	s_cbranch_execz .LBB3_12
	s_load_dwordx2 s[16:17], s[0:1], 0x10
	s_lshl_b32 s2, s4, 8
	s_addk_i32 s2, 0x1100
	v_cvt_pk_f16_f32 v53, v6, v7
	v_cvt_pk_f16_f32 v54, v8, v9
	v_cvt_pk_f16_f32 v55, v2, v3
	v_cvt_pk_f16_f32 v56, v4, v5
	s_mov_b32 s19, 0x20000
	s_mov_b32 s18, 0x186a000
	s_waitcnt lgkmcnt(0)
	s_and_b32 s17, s17, 0xffff
	v_lshl_or_b32 v57, v43, 2, s2
	v_lshl_or_b32 v58, v45, 2, s2
	v_sub_u32_e32 v59, v48, v51
	v_add_u32_e32 v60, -9, v48
	v_add_u32_e32 v61, -1, v48
	v_mov_b32_e32 v41, 0
	v_mov_b32_e32 v62, 0xff800000
	s_mov_b64 s[30:31], 0
	v_bfrev_b32_e32 v63, 1
	v_mov_b32_e32 v65, 0xff800000
	v_mov_b32_e32 v64, 0
	v_mov_b32_e32 v38, 0
	v_mov_b32_e32 v39, 0
	v_mov_b32_e32 v36, 0
	v_mov_b32_e32 v37, 0
	v_mov_b32_e32 v34, 0
	v_mov_b32_e32 v35, 0
	v_mov_b32_e32 v32, 0
	v_mov_b32_e32 v33, 0
	s_branch .LBB3_5

.LBB3_12:
	s_or_b64 exec, exec, s[28:29]
	v_lshlrev_b32_e32 v8, 2, v49
	s_load_dwordx2 s[2:3], s[0:1], 0x48
	s_load_dwordx2 s[6:7], s[0:1], 0x30
	s_waitcnt lgkmcnt(0)
	v_rcp_f32_e32 v8, v64
	s_cmp_lt_u32 s36, 64
	s_movk_i32 s0, 0x110
	s_cselect_b64 s[4:5], -1, 0
	v_cndmask_b32_e32 v8, 0, v8, vcc
	v_mad_i32_i24 v16, v46, s0, v47
	s_and_b64 s[0:1], exec, s[4:5]
	s_waitcnt vmcnt(1)
	v_pk_fma_f32 v[0:1], v[38:39], v[8:9], v[78:79] op_sel_hi:[1,0,1]
	v_pk_fma_f32 v[2:3], v[36:37], v[8:9], v[80:81] op_sel_hi:[1,0,1]
	s_waitcnt vmcnt(0)
	v_pk_fma_f32 v[4:5], v[34:35], v[8:9], v[82:83] op_sel_hi:[1,0,1]
	v_pk_fma_f32 v[6:7], v[32:33], v[8:9], v[84:85] op_sel_hi:[1,0,1]
	v_mul_f32_e32 v8, 0x3fb8aa3b, v0
	v_mul_f32_e32 v9, 0x3fb8aa3b, v1
	v_exp_f32_e32 v8, v8
	v_exp_f32_e32 v9, v9
	v_mul_f32_e32 v10, 0x3fb8aa3b, v2
	v_mul_f32_e32 v11, 0x3fb8aa3b, v3
	v_exp_f32_e32 v10, v10
	v_exp_f32_e32 v11, v11
	v_mul_f32_e32 v12, 0x3fb8aa3b, v4
	v_mul_f32_e32 v13, 0x3fb8aa3b, v5
	v_exp_f32_e32 v12, v12
	v_exp_f32_e32 v13, v13
	v_pk_add_f32 v[8:9], v[8:9], -1.0 op_sel_hi:[1,0]
	v_cmp_lt_f32_e32 vcc, 0, v1
	v_mul_f32_e32 v14, 0x3fb8aa3b, v6
	v_mul_f32_e32 v15, 0x3fb8aa3b, v7
	v_cndmask_b32_e32 v1, v9, v1, vcc
	v_cmp_lt_f32_e32 vcc, 0, v0
	v_exp_f32_e32 v14, v14
	v_exp_f32_e32 v15, v15
	v_pk_add_f32 v[10:11], v[10:11], -1.0 op_sel_hi:[1,0]
	v_cndmask_b32_e32 v0, v8, v0, vcc
	v_cmp_lt_f32_e32 vcc, 0, v3
	v_pk_add_f32 v[12:13], v[12:13], -1.0 op_sel_hi:[1,0]
	v_pk_add_f32 v[14:15], v[14:15], -1.0 op_sel_hi:[1,0]
	v_cndmask_b32_e32 v3, v11, v3, vcc
	v_cmp_lt_f32_e32 vcc, 0, v2
	v_cvt_pk_f16_f32 v0, v0, v1
	s_nop 0
	v_cndmask_b32_e32 v2, v10, v2, vcc
	v_cmp_lt_f32_e32 vcc, 0, v5
	v_cvt_pk_f16_f32 v1, v2, v3
	s_nop 0
	v_cndmask_b32_e32 v5, v13, v5, vcc
	v_cmp_lt_f32_e32 vcc, 0, v4
	s_nop 1
	v_cndmask_b32_e32 v4, v12, v4, vcc
	v_cmp_lt_f32_e32 vcc, 0, v7
	v_cvt_pk_f16_f32 v2, v4, v5
	s_nop 0
	v_cndmask_b32_e32 v7, v15, v7, vcc
	v_cmp_lt_f32_e32 vcc, 0, v6
	s_nop 1
	v_cndmask_b32_e32 v6, v14, v6, vcc
	v_cvt_pk_f16_f32 v3, v6, v7
	s_mov_b64 vcc, s[0:1]
	ds_write_b128 v16, v[0:3]
	s_cbranch_vccz .LBB3_14
	v_lshlrev_b32_e32 v16, 4, v42
	v_mov_b32_e32 v17, 0
	v_mul_u32_u24_e32 v2, 0x88, v44
	v_lshl_add_u64 v[0:1], s[6:7], 0, v[16:17]
	v_lshlrev_b32_e32 v2, 1, v2
	v_mov_b32_e32 v3, v17
	v_lshl_add_u64 v[18:19], v[0:1], 0, v[2:3]
	v_add_co_u32_e32 v40, vcc, 0x1000, v18
	s_nop 1
	v_addc_co_u32_e32 v41, vcc, 0, v19, vcc
	global_load_dwordx4 v[36:39], v[18:19], off
	global_load_dwordx4 v[28:31], v[18:19], off offset:64
	global_load_dwordx4 v[32:35], v[40:41], off offset:256
	global_load_dwordx4 v[20:23], v[40:41], off offset:320
	global_load_dwordx4 v[12:15], v[18:19], off offset:128
	global_load_dwordx4 v[8:11], v[18:19], off offset:192
	global_load_dwordx4 v[4:7], v[40:41], off offset:384
	global_load_dwordx4 v[0:3], v[40:41], off offset:448
	global_load_dwordx4 v[24:27], v16, s[22:23]
	s_nop 0
	global_load_dwordx4 v[16:19], v16, s[22:23] offset:64
	s_branch .LBB3_15

	.amdhsa_kernel _Z6k_agg1PKiS0_PK6__halfPKfS5_S5_S3_S5_S5_PS1_PfS7_S5_S0_S0_
		.amdhsa_group_segment_fixed_size 5376
		.amdhsa_private_segment_fixed_size 0
		.amdhsa_kernarg_size 120
		.amdhsa_user_sgpr_count 2
		.amdhsa_user_sgpr_dispatch_ptr 0
		.amdhsa_user_sgpr_queue_ptr 0
		.amdhsa_user_sgpr_kernarg_segment_ptr 1
		.amdhsa_user_sgpr_dispatch_id 0
		.amdhsa_user_sgpr_kernarg_preload_length 0
		.amdhsa_user_sgpr_kernarg_preload_offset 0
		.amdhsa_user_sgpr_private_segment_size 0
		.amdhsa_uses_dynamic_stack 0
		.amdhsa_enable_private_segment 0
		.amdhsa_system_sgpr_workgroup_id_x 1
		.amdhsa_system_sgpr_workgroup_id_y 0
		.amdhsa_system_sgpr_workgroup_id_z 0
		.amdhsa_system_sgpr_workgroup_info 0
		.amdhsa_system_vgpr_workitem_id 0
		.amdhsa_next_free_vgpr 87
		.amdhsa_next_free_sgpr 37
		.amdhsa_accum_offset 88
		.amdhsa_reserve_vcc 1
		.amdhsa_float_round_mode_32 0
		.amdhsa_float_round_mode_16_64 0
		.amdhsa_float_denorm_mode_32 3
		.amdhsa_float_denorm_mode_16_64 3
		.amdhsa_dx10_clamp 1
		.amdhsa_ieee_mode 1
		.amdhsa_fp16_overflow 0
		.amdhsa_tg_split 0
		.amdhsa_exception_fp_ieee_invalid_op 0
		.amdhsa_exception_fp_denorm_src 0
		.amdhsa_exception_fp_ieee_div_zero 0
		.amdhsa_exception_fp_ieee_overflow 0
		.amdhsa_exception_fp_ieee_underflow 0
		.amdhsa_exception_fp_ieee_inexact 0
		.amdhsa_exception_int_div_zero 0
	.end_amdhsa_kernel

amdhsa.kernels:
  - .agpr_count:     0
    .args:
      - .actual_access:  read_only
        .address_space:  global
        .offset:         0
        .size:           8
        .value_kind:     global_buffer
      - .actual_access:  read_only
        .address_space:  global
        .offset:         8
        .size:           8
        .value_kind:     global_buffer
      - .actual_access:  write_only
        .address_space:  global
        .offset:         16
        .size:           8
        .value_kind:     global_buffer
      - .actual_access:  write_only
        .address_space:  global
        .offset:         24
        .size:           8
        .value_kind:     global_buffer
      - .actual_access:  write_only
        .address_space:  global
        .offset:         32
        .size:           8
        .value_kind:     global_buffer
    .group_segment_fixed_size: 0
    .kernarg_segment_align: 8
    .kernarg_segment_size: 40
    .language:       OpenCL C
    .language_version:
      - 2
      - 0
    .max_flat_workgroup_size: 256
    .name:           _Z6k_prepPKfS0_P6__halfS2_Pi
    .private_segment_fixed_size: 0
    .sgpr_count:     18
    .sgpr_spill_count: 0
    .symbol:         _Z6k_prepPKfS0_P6__halfS2_Pi.kd
    .uniform_work_group_size: 1
    .uses_dynamic_stack: false
    .vgpr_count:     6
    .vgpr_spill_count: 0
    .wavefront_size: 64
  - .agpr_count:     0
    .args:
      - .actual_access:  read_only
        .address_space:  global
        .offset:         0
        .size:           8
        .value_kind:     global_buffer
      - .actual_access:  read_only
        .address_space:  global
        .offset:         8
        .size:           8
        .value_kind:     global_buffer
      - .address_space:  global
        .offset:         16
        .size:           8
        .value_kind:     global_buffer
      - .actual_access:  write_only
        .address_space:  global
        .offset:         24
        .size:           8
        .value_kind:     global_buffer
      - .actual_access:  write_only
        .address_space:  global
        .offset:         32
        .size:           8
        .value_kind:     global_buffer
      - .actual_access:  read_only
        .address_space:  global
        .offset:         40
        .size:           8
        .value_kind:     global_buffer
      - .actual_access:  read_only
        .address_space:  global
        .offset:         48
        .size:           8
        .value_kind:     global_buffer
      - .actual_access:  read_only
        .address_space:  global
        .offset:         56
        .size:           8
        .value_kind:     global_buffer
      - .actual_access:  read_only
        .address_space:  global
        .offset:         64
        .size:           8
        .value_kind:     global_buffer
      - .actual_access:  write_only
        .address_space:  global
        .offset:         72
        .size:           8
        .value_kind:     global_buffer
      - .actual_access:  read_only
        .address_space:  global
        .offset:         80
        .size:           8
        .value_kind:     global_buffer
      - .actual_access:  write_only
        .address_space:  global
        .offset:         88
        .size:           8
        .value_kind:     global_buffer
    .group_segment_fixed_size: 53248
    .kernarg_segment_align: 8
    .kernarg_segment_size: 96
    .language:       OpenCL C
    .language_version:
      - 2
      - 0
    .max_flat_workgroup_size: 256
    .name:           _Z15k_scatter_gemm1PKiS0_PiPjPyPKfPK6__halfS5_S5_PS6_PfSA_
    .private_segment_fixed_size: 0
    .sgpr_count:     32
    .sgpr_spill_count: 0
    .symbol:         _Z15k_scatter_gemm1PKiS0_PiPjPyPKfPK6__halfS5_S5_PS6_PfSA_.kd
    .uniform_work_group_size: 1
    .uses_dynamic_stack: false
    .vgpr_count:     146
    .vgpr_spill_count: 0
    .wavefront_size: 64
  - .agpr_count:     0
    .args:
      - .actual_access:  read_only
        .address_space:  global
        .offset:         0
        .size:           8
        .value_kind:     global_buffer
      - .actual_access:  read_only
        .address_space:  global
        .offset:         8
        .size:           8
        .value_kind:     global_buffer
      - .actual_access:  read_only
        .address_space:  global
        .offset:         16
        .size:           8
        .value_kind:     global_buffer
      - .actual_access:  write_only
        .address_space:  global
        .offset:         24
        .size:           8
        .value_kind:     global_buffer
      - .actual_access:  write_only
        .address_space:  global
        .offset:         32
        .size:           8
        .value_kind:     global_buffer
      - .actual_access:  write_only
        .address_space:  global
        .offset:         40
        .size:           8
        .value_kind:     global_buffer
      - .actual_access:  write_only
        .address_space:  global
        .offset:         48
        .size:           8
        .value_kind:     global_buffer
      - .actual_access:  read_only
        .address_space:  global
        .offset:         56
        .size:           8
        .value_kind:     global_buffer
      - .actual_access:  read_only
        .address_space:  global
        .offset:         64
        .size:           8
        .value_kind:     global_buffer
      - .actual_access:  read_only
        .address_space:  global
        .offset:         72
        .size:           8
        .value_kind:     global_buffer
      - .actual_access:  read_only
        .address_space:  global
        .offset:         80
        .size:           8
        .value_kind:     global_buffer
      - .actual_access:  write_only
        .address_space:  global
        .offset:         88
        .size:           8
        .value_kind:     global_buffer
      - .actual_access:  read_only
        .address_space:  global
        .offset:         96
        .size:           8
        .value_kind:     global_buffer
      - .actual_access:  write_only
        .address_space:  global
        .offset:         104
        .size:           8
        .value_kind:     global_buffer
    .group_segment_fixed_size: 53248
    .kernarg_segment_align: 8
    .kernarg_segment_size: 112
    .language:       OpenCL C
    .language_version:
      - 2
      - 0
    .max_flat_workgroup_size: 256
    .name:           _Z12k_fine_gemm1PKjPKyPKiPiS5_S5_S5_PKfPK6__halfS7_S7_PS8_PfSC_
    .private_segment_fixed_size: 0
    .sgpr_count:     102
    .sgpr_spill_count: 0
    .symbol:         _Z12k_fine_gemm1PKjPKyPKiPiS5_S5_S5_PKfPK6__halfS7_S7_PS8_PfSC_.kd
    .uniform_work_group_size: 1
    .uses_dynamic_stack: false
    .vgpr_count:     144
    .vgpr_spill_count: 0
    .wavefront_size: 64
  - .agpr_count:     0
    .args:
      - .actual_access:  read_only
        .address_space:  global
        .offset:         0
        .size:           8
        .value_kind:     global_buffer
      - .actual_access:  read_only
        .address_space:  global
        .offset:         8
        .size:           8
        .value_kind:     global_buffer
      - .actual_access:  read_only
        .address_space:  global
        .offset:         16
        .size:           8
        .value_kind:     global_buffer
      - .actual_access:  read_only
        .address_space:  global
        .offset:         24
        .size:           8
        .value_kind:     global_buffer
      - .actual_access:  read_only
        .address_space:  global
        .offset:         32
        .size:           8
        .value_kind:     global_buffer
      - .actual_access:  read_only
        .address_space:  global
        .offset:         40
        .size:           8
        .value_kind:     global_buffer
      - .actual_access:  read_only
        .address_space:  global
        .offset:         48
        .size:           8
        .value_kind:     global_buffer
      - .actual_access:  read_only
        .address_space:  global
        .offset:         56
        .size:           8
        .value_kind:     global_buffer
      - .actual_access:  read_only
        .address_space:  global
        .offset:         64
        .size:           8
        .value_kind:     global_buffer
      - .actual_access:  write_only
        .address_space:  global
        .offset:         72
        .size:           8
        .value_kind:     global_buffer
      - .actual_access:  read_only
        .address_space:  global
        .offset:         80
        .size:           8
        .value_kind:     global_buffer
      - .actual_access:  write_only
        .address_space:  global
        .offset:         88
        .size:           8
        .value_kind:     global_buffer
      - .actual_access:  read_only
        .address_space:  global
        .offset:         96
        .size:           8
        .value_kind:     global_buffer
      - .actual_access:  read_only
        .address_space:  global
        .offset:         104
        .size:           8
        .value_kind:     global_buffer
      - .actual_access:  read_only
        .address_space:  global
        .offset:         112
        .size:           8
        .value_kind:     global_buffer
    .group_segment_fixed_size: 5376
    .kernarg_segment_align: 8
    .kernarg_segment_size: 120
    .language:       OpenCL C
    .language_version:
      - 2
      - 0
    .max_flat_workgroup_size: 256
    .name:           _Z6k_agg1PKiS0_PK6__halfPKfS5_S5_S3_S5_S5_PS1_PfS7_S5_S0_S0_
    .private_segment_fixed_size: 0
    .sgpr_count:     43
    .sgpr_spill_count: 0
    .symbol:         _Z6k_agg1PKiS0_PK6__halfPKfS5_S5_S3_S5_S5_PS1_PfS7_S5_S0_S0_.kd
    .uniform_work_group_size: 1
    .uses_dynamic_stack: false
    .vgpr_count:     87
    .vgpr_spill_count: 0
    .wavefront_size: 64
  - .agpr_count:     0
    .args:
      - .actual_access:  read_only
        .address_space:  global
        .offset:         0
        .size:           8
        .value_kind:     global_buffer
      - .actual_access:  read_only
        .address_space:  global
        .offset:         8
        .size:           8
        .value_kind:     global_buffer
      - .actual_access:  read_only
        .address_space:  global
        .offset:         16
        .size:           8
        .value_kind:     global_buffer
      - .actual_access:  read_only
        .address_space:  global
        .offset:         24
        .size:           8
        .value_kind:     global_buffer
      - .actual_access:  read_only
        .address_space:  global
        .offset:         32
        .size:           8
        .value_kind:     global_buffer
      - .actual_access:  read_only
        .address_space:  global
        .offset:         40
        .size:           8
        .value_kind:     global_buffer
      - .actual_access:  write_only
        .address_space:  global
        .offset:         48
        .size:           8
        .value_kind:     global_buffer
      - .actual_access:  read_only
        .address_space:  global
        .offset:         56
        .size:           8
        .value_kind:     global_buffer
      - .actual_access:  read_only
        .address_space:  global
        .offset:         64
        .size:           8
        .value_kind:     global_buffer
      - .actual_access:  read_only
        .address_space:  global
        .offset:         72
        .size:           8
        .value_kind:     global_buffer
    .group_segment_fixed_size: 1024
    .kernarg_segment_align: 8
    .kernarg_segment_size: 80
    .language:       OpenCL C
    .language_version:
      - 2
      - 0
    .max_flat_workgroup_size: 256
    .name:           _Z6k_agg2PKiS0_PK6__halfPKfS5_S5_PfS5_S0_S0_
    .private_segment_fixed_size: 0
    .sgpr_count:     28
    .sgpr_spill_count: 0
    .symbol:         _Z6k_agg2PKiS0_PK6__halfPKfS5_S5_PfS5_S0_S0_.kd
    .uniform_work_group_size: 1
    .uses_dynamic_stack: false
    .vgpr_count:     60
    .vgpr_spill_count: 0
    .wavefront_size: 64
